# attention fast path: fq+-2 screening (loads + dots + check) moved after the output stores so it overlaps the store drain
# speedup vs baseline: 1.1961x; 1.0009x over previous
_Z8attn_fwdPKDF16_S0_S0_PKjPf:
	s_mov_b64 s[36:37], s[0:1]
	s_mov_b32 s38, s2
	s_load_dwordx4 s[8:11], s[0:1], 0x0
	s_load_dwordx4 s[12:15], s[0:1], 0x10
	s_load_dwordx2 s[16:17], s[0:1], 0x20
	s_lshl_b32 s3, s2, 1
	s_mul_hi_u32 s4, s2, 0xaaaaaaab
	s_and_b32 s3, s3, 14
	s_lshr_b32 s4, s4, 6
	s_add_i32 s6, s3, s4
	s_lshr_b32 s5, s2, 3
	s_mul_hi_u32 s7, s5, 0x15555556
	s_mul_i32 s7, s7, 12
	s_sub_i32 s20, s5, s7
	v_and_b32_e32 v1, 63, v0
	v_readfirstlane_b32 s19, v0
	v_and_b32_e32 v2, 3, v1
	v_lshrrev_b32_e32 v3, 2, v1
	s_lshr_b32 s19, s19, 6
	s_lshl_b32 s18, s19, 5
	s_lshl_b32 s26, s19, 12
	v_lshl_add_u32 v4, v1, 4, s26
	v_mul_u32_u24_e32 v5, 0x6000, v3
	v_lshl_add_u32 v5, v2, 4, v5
	v_add_u32_e32 v6, 0x1800, v5
	v_add_u32_e32 v7, 0x3000, v5
	v_add_u32_e32 v8, 0x4800, v5
	v_min_u32_e32 v9, 47, v1
	v_lshlrev_b32_e32 v9, 2, v9
	s_mul_i32 s21, s6, 0xc00
	s_cmp_lt_u32 s20, 11
	s_cselect_b32 s22, 1, 0
	s_cselect_b32 s40, 0, 0xf149f2ca
	s_add_i32 s22, s20, s22
	s_cmp_gt_u32 s20, 0
	s_cselect_b32 s23, 1, 0
	s_cselect_b32 s41, 0, 0xf149f2ca
	s_sub_i32 s23, s20, s23
	s_cmp_lt_u32 s20, 10
	s_cselect_b32 s24, 2, 0
	s_cselect_b32 s42, 0, 0xf149f2ca
	s_add_i32 s24, s20, s24
	s_cmp_gt_u32 s20, 1
	s_cselect_b32 s25, 2, 0
	s_cselect_b32 s43, 0, 0xf149f2ca
	s_sub_i32 s25, s20, s25
	s_waitcnt lgkmcnt(0)
	s_lshl_b32 s26, s20, 8
	s_add_i32 s26, s26, s21
	s_lshl_b32 s26, s26, 7
	s_add_u32 s44, s10, s26
	s_addc_u32 s45, s11, 0
	s_add_u32 s54, s8, s26
	s_addc_u32 s55, s9, 0
	s_lshl_b32 s27, s20, 8
	s_add_i32 s27, s27, s21
	s_add_i32 s27, s27, s18
	s_lshl_b32 s27, s27, 8
	s_add_u32 s62, s16, s27
	s_addc_u32 s63, s17, 0
	s_lshl_b32 s26, s22, 8
	s_add_i32 s26, s26, s21
	s_lshl_b32 s26, s26, 7
	s_add_u32 s46, s10, s26
	s_addc_u32 s47, s11, 0
	s_lshl_b32 s26, s23, 8
	s_add_i32 s26, s26, s21
	s_lshl_b32 s26, s26, 7
	s_add_u32 s48, s10, s26
	s_addc_u32 s49, s11, 0
	s_lshl_b32 s26, s24, 8
	s_add_i32 s26, s26, s21
	s_lshl_b32 s26, s26, 7
	s_add_u32 s50, s10, s26
	s_addc_u32 s51, s11, 0
	s_lshl_b32 s26, s25, 8
	s_add_i32 s26, s26, s21
	s_lshl_b32 s26, s26, 7
	s_add_u32 s52, s10, s26
	s_addc_u32 s53, s11, 0
	s_mul_i32 s28, s6, 0x30000
	s_add_i32 s28, s28, s18
	s_lshl_b32 s26, s20, 8
	s_add_i32 s26, s26, s28
	s_lshl_b32 s26, s26, 1
	s_add_u32 s56, s12, s26
	s_addc_u32 s57, s13, 0
	s_lshl_b32 s26, s22, 8
	s_add_i32 s26, s26, s28
	s_lshl_b32 s26, s26, 1
	s_add_u32 s58, s12, s26
	s_addc_u32 s59, s13, 0
	s_lshl_b32 s26, s23, 8
	s_add_i32 s26, s26, s28
	s_lshl_b32 s26, s26, 1
	s_add_u32 s60, s12, s26
	s_addc_u32 s61, s13, 0
	s_mul_i32 s26, s6, 0xc0
	s_add_u32 s64, s14, s26
	s_addc_u32 s65, s15, 0
	global_load_dword v10, v9, s[64:65]
	global_load_dwordx4 v[96:99], v4, s[54:55] nt
	global_load_dwordx4 v[100:103], v4, s[54:55] offset:1024 nt
	global_load_dwordx4 v[104:107], v4, s[54:55] offset:2048 nt
	global_load_dwordx4 v[108:111], v4, s[54:55] offset:3072 nt
	global_load_dwordx4 v[112:115], v4, s[44:45]
	global_load_dwordx4 v[116:119], v4, s[44:45] offset:1024
	global_load_dwordx4 v[120:123], v4, s[44:45] offset:2048
	global_load_dwordx4 v[124:127], v4, s[44:45] offset:3072
	global_load_dwordx4 v[128:131], v4, s[46:47]
	global_load_dwordx4 v[132:135], v4, s[46:47] offset:1024
	global_load_dwordx4 v[136:139], v4, s[46:47] offset:2048
	global_load_dwordx4 v[140:143], v4, s[46:47] offset:3072
	global_load_dwordx4 v[144:147], v4, s[48:49]
	global_load_dwordx4 v[148:151], v4, s[48:49] offset:1024
	global_load_dwordx4 v[152:155], v4, s[48:49] offset:2048
	global_load_dwordx4 v[156:159], v4, s[48:49] offset:3072
	global_load_dwordx4 v[192:195], v5, s[56:57]
	global_load_dwordx4 v[196:199], v6, s[56:57]
	global_load_dwordx4 v[200:203], v7, s[56:57]
	global_load_dwordx4 v[204:207], v8, s[56:57]
	global_load_dwordx4 v[208:211], v5, s[58:59]
	global_load_dwordx4 v[212:215], v6, s[58:59]
	global_load_dwordx4 v[216:219], v7, s[58:59]
	global_load_dwordx4 v[220:223], v8, s[58:59]
	global_load_dwordx4 v[224:227], v5, s[60:61]
	global_load_dwordx4 v[228:231], v6, s[60:61]
	global_load_dwordx4 v[232:235], v7, s[60:61]
	global_load_dwordx4 v[236:239], v8, s[60:61]
	global_load_dwordx4 v[160:163], v4, s[50:51]
	global_load_dwordx4 v[164:167], v4, s[50:51] offset:1024
	global_load_dwordx4 v[168:171], v4, s[50:51] offset:2048
	global_load_dwordx4 v[172:175], v4, s[50:51] offset:3072
	global_load_dwordx4 v[176:179], v4, s[52:53]
	global_load_dwordx4 v[180:183], v4, s[52:53] offset:1024
	global_load_dwordx4 v[184:187], v4, s[52:53] offset:2048
	global_load_dwordx4 v[188:191], v4, s[52:53] offset:3072
	s_waitcnt vmcnt(32)
	v_max_f32_dpp v11, v10, v10 quad_perm:[1,0,3,2] row_mask:0xf bank_mask:0xf
	v_dot2_f32_f16 v64, v96, v96, 0
	v_dot2_f32_f16 v65, v100, v100, 0
	v_dot2_f32_f16 v66, v104, v104, 0
	v_dot2_f32_f16 v67, v108, v108, 0
	v_max_f32_dpp v11, v11, v11 quad_perm:[2,3,0,1] row_mask:0xf bank_mask:0xf
	v_dot2_f32_f16 v64, v97, v97, v64
	v_dot2_f32_f16 v65, v101, v101, v65
	v_dot2_f32_f16 v66, v105, v105, v66
	v_dot2_f32_f16 v67, v109, v109, v67
	v_max_f32_dpp v11, v11, v11 row_half_mirror row_mask:0xf bank_mask:0xf
	v_dot2_f32_f16 v64, v98, v98, v64
	v_dot2_f32_f16 v65, v102, v102, v65
	v_dot2_f32_f16 v66, v106, v106, v66
	v_dot2_f32_f16 v67, v110, v110, v67
	v_max_f32_dpp v11, v11, v11 row_mirror row_mask:0xf bank_mask:0xf
	v_dot2_f32_f16 v64, v99, v99, v64
	v_dot2_f32_f16 v65, v103, v103, v65
	v_dot2_f32_f16 v66, v107, v107, v66
	v_dot2_f32_f16 v67, v111, v111, v67
	s_nop 2
	v_add_f32_dpp v64, v64, v64 quad_perm:[1,0,3,2] row_mask:0xf bank_mask:0xf
	v_add_f32_dpp v65, v65, v65 quad_perm:[1,0,3,2] row_mask:0xf bank_mask:0xf
	v_add_f32_dpp v66, v66, v66 quad_perm:[1,0,3,2] row_mask:0xf bank_mask:0xf
	v_add_f32_dpp v67, v67, v67 quad_perm:[1,0,3,2] row_mask:0xf bank_mask:0xf
	v_add_f32_dpp v64, v64, v64 quad_perm:[2,3,0,1] row_mask:0xf bank_mask:0xf
	v_add_f32_dpp v65, v65, v65 quad_perm:[2,3,0,1] row_mask:0xf bank_mask:0xf
	v_add_f32_dpp v66, v66, v66 quad_perm:[2,3,0,1] row_mask:0xf bank_mask:0xf
	v_add_f32_dpp v67, v67, v67 quad_perm:[2,3,0,1] row_mask:0xf bank_mask:0xf
	v_add_f32_dpp v64, v64, v64 row_half_mirror row_mask:0xf bank_mask:0xf
	v_add_f32_dpp v65, v65, v65 row_half_mirror row_mask:0xf bank_mask:0xf
	v_add_f32_dpp v66, v66, v66 row_half_mirror row_mask:0xf bank_mask:0xf
	v_add_f32_dpp v67, v67, v67 row_half_mirror row_mask:0xf bank_mask:0xf
	v_max3_f32 v68, v64, v65, v66
	v_readlane_b32 s26, v11, 0
	v_max_f32_e32 v68, v68, v67
	v_readlane_b32 s27, v11, 16
	v_readlane_b32 s28, v11, 32
	v_max_f32_dpp v68, v68, v68 row_mirror row_mask:0xf bank_mask:0xf
	v_readlane_b32 s29, v11, 48
	v_mov_b32_e32 v69, s26
	v_max_f32_e32 v69, s27, v69
	v_max_f32_e32 v69, s28, v69
	v_max_f32_e32 v69, s29, v69
	v_readlane_b32 s26, v68, 0
	v_readlane_b32 s27, v68, 16
	v_readlane_b32 s28, v68, 32
	v_readlane_b32 s29, v68, 48
	v_sqrt_f32_e32 v69, v69
	v_mov_b32_e32 v70, s26
	v_max_f32_e32 v70, s27, v70
	v_max_f32_e32 v70, s28, v70
	v_max_f32_e32 v70, s29, v70
	v_mul_f32_e32 v69, 0x3f8020c5, v69
	v_sqrt_f32_e32 v70, v70
	s_nop 0
	v_mul_f32_e32 v70, 0x3f8020c5, v70
	v_mul_f32_e32 v69, v69, v70
	v_add_f32_e32 v69, 0x42191384, v69
	s_waitcnt vmcnt(28)
	v_dot2_f32_f16 v12, v96, v112, 0
	v_dot2_f32_f16 v13, v100, v116, 0
	v_dot2_f32_f16 v14, v104, v120, 0
	v_dot2_f32_f16 v15, v108, v124, 0
	v_dot2_f32_f16 v12, v97, v113, v12
	v_dot2_f32_f16 v13, v101, v117, v13
	v_dot2_f32_f16 v14, v105, v121, v14
	v_dot2_f32_f16 v15, v109, v125, v15
	v_dot2_f32_f16 v12, v98, v114, v12
	v_dot2_f32_f16 v13, v102, v118, v13
	v_dot2_f32_f16 v14, v106, v122, v14
	v_dot2_f32_f16 v15, v110, v126, v15
	v_dot2_f32_f16 v12, v99, v115, v12
	v_dot2_f32_f16 v13, v103, v119, v13
	v_dot2_f32_f16 v14, v107, v123, v14
	v_dot2_f32_f16 v15, v111, v127, v15
	s_waitcnt vmcnt(24)
	v_dot2_f32_f16 v16, v96, v128, 0
	v_dot2_f32_f16 v17, v100, v132, 0
	v_dot2_f32_f16 v18, v104, v136, 0
	v_dot2_f32_f16 v19, v108, v140, 0
	v_dot2_f32_f16 v16, v97, v129, v16
	v_dot2_f32_f16 v17, v101, v133, v17
	v_dot2_f32_f16 v18, v105, v137, v18
	v_dot2_f32_f16 v19, v109, v141, v19
	v_dot2_f32_f16 v16, v98, v130, v16
	v_dot2_f32_f16 v17, v102, v134, v17
	v_dot2_f32_f16 v18, v106, v138, v18
	v_dot2_f32_f16 v19, v110, v142, v19
	v_dot2_f32_f16 v16, v99, v131, v16
	v_dot2_f32_f16 v17, v103, v135, v17
	v_dot2_f32_f16 v18, v107, v139, v18
	v_dot2_f32_f16 v19, v111, v143, v19
	s_waitcnt vmcnt(20)
	v_dot2_f32_f16 v20, v96, v144, 0
	v_dot2_f32_f16 v21, v100, v148, 0
	v_dot2_f32_f16 v22, v104, v152, 0
	v_dot2_f32_f16 v23, v108, v156, 0
	v_dot2_f32_f16 v20, v97, v145, v20
	v_dot2_f32_f16 v21, v101, v149, v21
	v_dot2_f32_f16 v22, v105, v153, v22
	v_dot2_f32_f16 v23, v109, v157, v23
	v_dot2_f32_f16 v20, v98, v146, v20
	v_dot2_f32_f16 v21, v102, v150, v21
	v_dot2_f32_f16 v22, v106, v154, v22
	v_dot2_f32_f16 v23, v110, v158, v23
	v_dot2_f32_f16 v20, v99, v147, v20
	v_dot2_f32_f16 v21, v103, v151, v21
	v_dot2_f32_f16 v22, v107, v155, v22
	v_dot2_f32_f16 v23, v111, v159, v23
	s_nop 2
	v_add_f32_dpp v12, v12, v12 quad_perm:[1,0,3,2] row_mask:0xf bank_mask:0xf
	v_add_f32_dpp v13, v13, v13 quad_perm:[1,0,3,2] row_mask:0xf bank_mask:0xf
	v_add_f32_dpp v14, v14, v14 quad_perm:[1,0,3,2] row_mask:0xf bank_mask:0xf
	v_add_f32_dpp v15, v15, v15 quad_perm:[1,0,3,2] row_mask:0xf bank_mask:0xf
	v_add_f32_dpp v16, v16, v16 quad_perm:[1,0,3,2] row_mask:0xf bank_mask:0xf
	v_add_f32_dpp v17, v17, v17 quad_perm:[1,0,3,2] row_mask:0xf bank_mask:0xf
	v_add_f32_dpp v18, v18, v18 quad_perm:[1,0,3,2] row_mask:0xf bank_mask:0xf
	v_add_f32_dpp v19, v19, v19 quad_perm:[1,0,3,2] row_mask:0xf bank_mask:0xf
	v_add_f32_dpp v20, v20, v20 quad_perm:[1,0,3,2] row_mask:0xf bank_mask:0xf
	v_add_f32_dpp v21, v21, v21 quad_perm:[1,0,3,2] row_mask:0xf bank_mask:0xf
	v_add_f32_dpp v22, v22, v22 quad_perm:[1,0,3,2] row_mask:0xf bank_mask:0xf
	v_add_f32_dpp v23, v23, v23 quad_perm:[1,0,3,2] row_mask:0xf bank_mask:0xf
	v_add_f32_dpp v12, v12, v12 quad_perm:[2,3,0,1] row_mask:0xf bank_mask:0xf
	v_add_f32_dpp v13, v13, v13 quad_perm:[2,3,0,1] row_mask:0xf bank_mask:0xf
	v_add_f32_dpp v14, v14, v14 quad_perm:[2,3,0,1] row_mask:0xf bank_mask:0xf
	v_add_f32_dpp v15, v15, v15 quad_perm:[2,3,0,1] row_mask:0xf bank_mask:0xf
	v_add_f32_dpp v16, v16, v16 quad_perm:[2,3,0,1] row_mask:0xf bank_mask:0xf
	v_add_f32_dpp v17, v17, v17 quad_perm:[2,3,0,1] row_mask:0xf bank_mask:0xf
	v_add_f32_dpp v18, v18, v18 quad_perm:[2,3,0,1] row_mask:0xf bank_mask:0xf
	v_add_f32_dpp v19, v19, v19 quad_perm:[2,3,0,1] row_mask:0xf bank_mask:0xf
	v_add_f32_dpp v20, v20, v20 quad_perm:[2,3,0,1] row_mask:0xf bank_mask:0xf
	v_add_f32_dpp v21, v21, v21 quad_perm:[2,3,0,1] row_mask:0xf bank_mask:0xf
	v_add_f32_dpp v22, v22, v22 quad_perm:[2,3,0,1] row_mask:0xf bank_mask:0xf
	v_add_f32_dpp v23, v23, v23 quad_perm:[2,3,0,1] row_mask:0xf bank_mask:0xf
	v_add_f32_dpp v12, v12, v12 row_half_mirror row_mask:0xf bank_mask:0xf
	v_add_f32_dpp v13, v13, v13 row_half_mirror row_mask:0xf bank_mask:0xf
	v_add_f32_dpp v14, v14, v14 row_half_mirror row_mask:0xf bank_mask:0xf
	v_add_f32_dpp v15, v15, v15 row_half_mirror row_mask:0xf bank_mask:0xf
	v_add_f32_dpp v16, v16, v16 row_half_mirror row_mask:0xf bank_mask:0xf
	v_add_f32_dpp v17, v17, v17 row_half_mirror row_mask:0xf bank_mask:0xf
	v_add_f32_dpp v18, v18, v18 row_half_mirror row_mask:0xf bank_mask:0xf
	v_add_f32_dpp v19, v19, v19 row_half_mirror row_mask:0xf bank_mask:0xf
	v_add_f32_dpp v20, v20, v20 row_half_mirror row_mask:0xf bank_mask:0xf
	v_add_f32_dpp v21, v21, v21 row_half_mirror row_mask:0xf bank_mask:0xf
	v_add_f32_dpp v22, v22, v22 row_half_mirror row_mask:0xf bank_mask:0xf
	v_add_f32_dpp v23, v23, v23 row_half_mirror row_mask:0xf bank_mask:0xf
	v_cmp_eq_u32_e64 s[70:71], 1, v2
	v_cmp_eq_u32_e64 s[72:73], 2, v2
	v_cmp_eq_u32_e64 s[74:75], 3, v2
	v_cndmask_b32_e64 v112, v12, v13, s[70:71]
	v_cndmask_b32_e64 v113, v16, v17, s[70:71]
	v_cndmask_b32_e64 v114, v20, v21, s[70:71]
	v_cndmask_b32_e64 v112, v112, v14, s[72:73]
	v_cndmask_b32_e64 v113, v113, v18, s[72:73]
	v_cndmask_b32_e64 v114, v114, v22, s[72:73]
	v_cndmask_b32_e64 v112, v112, v15, s[74:75]
	v_cndmask_b32_e64 v113, v113, v19, s[74:75]
	v_cndmask_b32_e64 v114, v114, v23, s[74:75]
	v_add_f32_e32 v112, 0x42e59caf, v112
	v_add_f32_e32 v113, 0x42e59caf, v113
	v_add_f32_e32 v114, 0x42e59caf, v114
	v_add_f32_e32 v113, s40, v113
	v_add_f32_e32 v114, s41, v114
	v_max3_f32 v117, v112, v113, v114
	v_sub_f32_e32 v120, v112, v117
	v_sub_f32_e32 v121, v113, v117
	v_sub_f32_e32 v122, v114, v117
	v_exp_f32_e32 v120, v120
	v_exp_f32_e32 v121, v121
	v_exp_f32_e32 v122, v122
	v_min_f32_dpp v119, v117, v117 quad_perm:[1,0,3,2] row_mask:0xf bank_mask:0xf
	s_mov_b32 s30, 0xc2200a3d
	s_mov_b32 s31, 0
	v_min_f32_dpp v119, v119, v119 quad_perm:[2,3,0,1] row_mask:0xf bank_mask:0xf
	s_nop 0
	s_nop 0
	v_min_f32_dpp v119, v119, v119 row_half_mirror row_mask:0xf bank_mask:0xf
	v_add_f32_e32 v123, v120, v121
	v_add_f32_e32 v123, v123, v122
	v_min_f32_dpp v119, v119, v119 row_mirror row_mask:0xf bank_mask:0xf
	s_nop 1
	v_readlane_b32 s26, v119, 0
	v_readlane_b32 s27, v119, 16
	v_readlane_b32 s28, v119, 32
	v_readlane_b32 s29, v119, 48
	s_nop 1
	v_mov_b32_e32 v138, s26
	v_min_f32_e32 v138, s27, v138
	v_min_f32_e32 v138, s28, v138
	v_min_f32_e32 v138, s29, v138
	v_sub_f32_e32 v69, v69, v138
	v_cmp_ngt_f32_e32 vcc, s30, v69
	s_cmp_lg_u64 vcc, 0
	s_cselect_b32 s26, 1, 0
	s_or_b32 s31, s31, s26
	v_div_scale_f32 v141, s[26:27], v123, v123, 1.0
	v_rcp_f32_e32 v142, v141
	s_nop 0
	v_fma_f32 v143, -v141, v142, 1.0
	v_fmac_f32_e32 v142, v143, v142
	v_div_scale_f32 v143, vcc, 1.0, v123, 1.0
	v_mul_f32_e32 v144, v143, v142
	v_fma_f32 v145, -v141, v144, v143
	v_fmac_f32_e32 v144, v145, v142
	v_fma_f32 v141, -v141, v144, v143
	v_div_fmas_f32 v141, v141, v142, v144
	v_div_fixup_f32 v123, v141, v123, 1.0
	v_mul_f32_e32 v120, v120, v123
	v_mul_f32_e32 v121, v121, v123
	v_mul_f32_e32 v122, v122, v123
	v_lshrrev_b32_e32 v152, 3, v1
	v_and_b32_e32 v153, 3, v152
	v_lshrrev_b32_e32 v152, 2, v152
	v_lshlrev_b32_e32 v152, 5, v152
	v_lshl_or_b32 v152, v153, 2, v152
	v_and_b32_e32 v153, 1, v2
	v_lshl_or_b32 v152, v153, 4, v152
	v_lshrrev_b32_e32 v153, 1, v2
	v_lshl_or_b32 v152, v153, 6, v152
	s_lshl_b32 s26, s19, 9
	s_add_i32 s26, s26, 0x18000
	v_add_u32_e32 v152, s26, v152
	v_lshl_add_u32 v153, v2, 5, s26
	ds_write_b32 v152, v120
	ds_write_b32 v152, v121 offset:128
	ds_write_b32 v152, v122 offset:256
	ds_read_b128 v[64:67], v153
	ds_read_b128 v[68:71], v153 offset:16
	ds_read_b128 v[72:75], v153 offset:128
	ds_read_b128 v[76:79], v153 offset:144
	ds_read_b128 v[80:83], v153 offset:256
	ds_read_b128 v[84:87], v153 offset:272
	v_lshrrev_b32_e32 v154, 1, v2
	v_and_b32_e32 v155, 1, v2
	v_lshlrev_b32_e32 v154, 4, v154
	v_lshl_or_b32 v154, v155, 2, v154
	v_lshlrev_b32_e32 v154, 8, v154
	v_lshl_add_u32 v154, v3, 4, v154
	s_waitcnt lgkmcnt(0)
	s_waitcnt vmcnt(16)
	v_fma_mix_f32 v32, v192, v64, 0 op_sel:[0,0,0] op_sel_hi:[1,0,0]
	v_fma_mix_f32 v36, v192, v65, 0 op_sel:[1,0,0] op_sel_hi:[1,0,0]
	v_fma_mix_f32 v40, v193, v66, 0 op_sel:[0,0,0] op_sel_hi:[1,0,0]
	v_fma_mix_f32 v44, v193, v67, 0 op_sel:[1,0,0] op_sel_hi:[1,0,0]
	v_fma_mix_f32 v48, v194, v68, 0 op_sel:[0,0,0] op_sel_hi:[1,0,0]
	v_fma_mix_f32 v52, v194, v69, 0 op_sel:[1,0,0] op_sel_hi:[1,0,0]
	v_fma_mix_f32 v56, v195, v70, 0 op_sel:[0,0,0] op_sel_hi:[1,0,0]
	v_fma_mix_f32 v60, v195, v71, 0 op_sel:[1,0,0] op_sel_hi:[1,0,0]
	v_fma_mix_f32 v33, v196, v64, 0 op_sel:[0,0,0] op_sel_hi:[1,0,0]
	v_fma_mix_f32 v37, v196, v65, 0 op_sel:[1,0,0] op_sel_hi:[1,0,0]
	v_fma_mix_f32 v41, v197, v66, 0 op_sel:[0,0,0] op_sel_hi:[1,0,0]
	v_fma_mix_f32 v45, v197, v67, 0 op_sel:[1,0,0] op_sel_hi:[1,0,0]
	v_fma_mix_f32 v49, v198, v68, 0 op_sel:[0,0,0] op_sel_hi:[1,0,0]
	v_fma_mix_f32 v53, v198, v69, 0 op_sel:[1,0,0] op_sel_hi:[1,0,0]
	v_fma_mix_f32 v57, v199, v70, 0 op_sel:[0,0,0] op_sel_hi:[1,0,0]
	v_fma_mix_f32 v61, v199, v71, 0 op_sel:[1,0,0] op_sel_hi:[1,0,0]
	v_fma_mix_f32 v34, v200, v64, 0 op_sel:[0,0,0] op_sel_hi:[1,0,0]
	v_fma_mix_f32 v38, v200, v65, 0 op_sel:[1,0,0] op_sel_hi:[1,0,0]
	v_fma_mix_f32 v42, v201, v66, 0 op_sel:[0,0,0] op_sel_hi:[1,0,0]
	v_fma_mix_f32 v46, v201, v67, 0 op_sel:[1,0,0] op_sel_hi:[1,0,0]
	v_fma_mix_f32 v50, v202, v68, 0 op_sel:[0,0,0] op_sel_hi:[1,0,0]
	v_fma_mix_f32 v54, v202, v69, 0 op_sel:[1,0,0] op_sel_hi:[1,0,0]
	v_fma_mix_f32 v58, v203, v70, 0 op_sel:[0,0,0] op_sel_hi:[1,0,0]
	v_fma_mix_f32 v62, v203, v71, 0 op_sel:[1,0,0] op_sel_hi:[1,0,0]
	v_fma_mix_f32 v35, v204, v64, 0 op_sel:[0,0,0] op_sel_hi:[1,0,0]
	v_fma_mix_f32 v39, v204, v65, 0 op_sel:[1,0,0] op_sel_hi:[1,0,0]
	v_fma_mix_f32 v43, v205, v66, 0 op_sel:[0,0,0] op_sel_hi:[1,0,0]
	v_fma_mix_f32 v47, v205, v67, 0 op_sel:[1,0,0] op_sel_hi:[1,0,0]
	v_fma_mix_f32 v51, v206, v68, 0 op_sel:[0,0,0] op_sel_hi:[1,0,0]
	v_fma_mix_f32 v55, v206, v69, 0 op_sel:[1,0,0] op_sel_hi:[1,0,0]
	v_fma_mix_f32 v59, v207, v70, 0 op_sel:[0,0,0] op_sel_hi:[1,0,0]
	v_fma_mix_f32 v63, v207, v71, 0 op_sel:[1,0,0] op_sel_hi:[1,0,0]
	s_waitcnt vmcnt(12)
	v_fma_mix_f32 v32, v208, v72, v32 op_sel:[0,0,0] op_sel_hi:[1,0,0]
	v_fma_mix_f32 v36, v208, v73, v36 op_sel:[1,0,0] op_sel_hi:[1,0,0]
	v_fma_mix_f32 v40, v209, v74, v40 op_sel:[0,0,0] op_sel_hi:[1,0,0]
	v_fma_mix_f32 v44, v209, v75, v44 op_sel:[1,0,0] op_sel_hi:[1,0,0]
	v_fma_mix_f32 v48, v210, v76, v48 op_sel:[0,0,0] op_sel_hi:[1,0,0]
	v_fma_mix_f32 v52, v210, v77, v52 op_sel:[1,0,0] op_sel_hi:[1,0,0]
	v_fma_mix_f32 v56, v211, v78, v56 op_sel:[0,0,0] op_sel_hi:[1,0,0]
	v_fma_mix_f32 v60, v211, v79, v60 op_sel:[1,0,0] op_sel_hi:[1,0,0]
	v_fma_mix_f32 v33, v212, v72, v33 op_sel:[0,0,0] op_sel_hi:[1,0,0]
	v_fma_mix_f32 v37, v212, v73, v37 op_sel:[1,0,0] op_sel_hi:[1,0,0]
	v_fma_mix_f32 v41, v213, v74, v41 op_sel:[0,0,0] op_sel_hi:[1,0,0]
	v_fma_mix_f32 v45, v213, v75, v45 op_sel:[1,0,0] op_sel_hi:[1,0,0]
	v_fma_mix_f32 v49, v214, v76, v49 op_sel:[0,0,0] op_sel_hi:[1,0,0]
	v_fma_mix_f32 v53, v214, v77, v53 op_sel:[1,0,0] op_sel_hi:[1,0,0]
	v_fma_mix_f32 v57, v215, v78, v57 op_sel:[0,0,0] op_sel_hi:[1,0,0]
	v_fma_mix_f32 v61, v215, v79, v61 op_sel:[1,0,0] op_sel_hi:[1,0,0]
	v_fma_mix_f32 v34, v216, v72, v34 op_sel:[0,0,0] op_sel_hi:[1,0,0]
	v_fma_mix_f32 v38, v216, v73, v38 op_sel:[1,0,0] op_sel_hi:[1,0,0]
	v_fma_mix_f32 v42, v217, v74, v42 op_sel:[0,0,0] op_sel_hi:[1,0,0]
	v_fma_mix_f32 v46, v217, v75, v46 op_sel:[1,0,0] op_sel_hi:[1,0,0]
	v_fma_mix_f32 v50, v218, v76, v50 op_sel:[0,0,0] op_sel_hi:[1,0,0]
	v_fma_mix_f32 v54, v218, v77, v54 op_sel:[1,0,0] op_sel_hi:[1,0,0]
	v_fma_mix_f32 v58, v219, v78, v58 op_sel:[0,0,0] op_sel_hi:[1,0,0]
	v_fma_mix_f32 v62, v219, v79, v62 op_sel:[1,0,0] op_sel_hi:[1,0,0]
	v_fma_mix_f32 v35, v220, v72, v35 op_sel:[0,0,0] op_sel_hi:[1,0,0]
	v_fma_mix_f32 v39, v220, v73, v39 op_sel:[1,0,0] op_sel_hi:[1,0,0]
	v_fma_mix_f32 v43, v221, v74, v43 op_sel:[0,0,0] op_sel_hi:[1,0,0]
	v_fma_mix_f32 v47, v221, v75, v47 op_sel:[1,0,0] op_sel_hi:[1,0,0]
	v_fma_mix_f32 v51, v222, v76, v51 op_sel:[0,0,0] op_sel_hi:[1,0,0]
	v_fma_mix_f32 v55, v222, v77, v55 op_sel:[1,0,0] op_sel_hi:[1,0,0]
	v_fma_mix_f32 v59, v223, v78, v59 op_sel:[0,0,0] op_sel_hi:[1,0,0]
	v_fma_mix_f32 v63, v223, v79, v63 op_sel:[1,0,0] op_sel_hi:[1,0,0]
	s_waitcnt vmcnt(8)
	v_fma_mix_f32 v32, v224, v80, v32 op_sel:[0,0,0] op_sel_hi:[1,0,0]
	v_fma_mix_f32 v36, v224, v81, v36 op_sel:[1,0,0] op_sel_hi:[1,0,0]
	v_fma_mix_f32 v40, v225, v82, v40 op_sel:[0,0,0] op_sel_hi:[1,0,0]
	v_fma_mix_f32 v44, v225, v83, v44 op_sel:[1,0,0] op_sel_hi:[1,0,0]
	v_fma_mix_f32 v48, v226, v84, v48 op_sel:[0,0,0] op_sel_hi:[1,0,0]
	v_fma_mix_f32 v52, v226, v85, v52 op_sel:[1,0,0] op_sel_hi:[1,0,0]
	v_fma_mix_f32 v56, v227, v86, v56 op_sel:[0,0,0] op_sel_hi:[1,0,0]
	v_fma_mix_f32 v60, v227, v87, v60 op_sel:[1,0,0] op_sel_hi:[1,0,0]
	v_fma_mix_f32 v33, v228, v80, v33 op_sel:[0,0,0] op_sel_hi:[1,0,0]
	v_fma_mix_f32 v37, v228, v81, v37 op_sel:[1,0,0] op_sel_hi:[1,0,0]
	v_fma_mix_f32 v41, v229, v82, v41 op_sel:[0,0,0] op_sel_hi:[1,0,0]
	v_fma_mix_f32 v45, v229, v83, v45 op_sel:[1,0,0] op_sel_hi:[1,0,0]
	v_fma_mix_f32 v49, v230, v84, v49 op_sel:[0,0,0] op_sel_hi:[1,0,0]
	v_fma_mix_f32 v53, v230, v85, v53 op_sel:[1,0,0] op_sel_hi:[1,0,0]
	v_fma_mix_f32 v57, v231, v86, v57 op_sel:[0,0,0] op_sel_hi:[1,0,0]
	v_fma_mix_f32 v61, v231, v87, v61 op_sel:[1,0,0] op_sel_hi:[1,0,0]
	v_fma_mix_f32 v34, v232, v80, v34 op_sel:[0,0,0] op_sel_hi:[1,0,0]
	v_fma_mix_f32 v38, v232, v81, v38 op_sel:[1,0,0] op_sel_hi:[1,0,0]
	v_fma_mix_f32 v42, v233, v82, v42 op_sel:[0,0,0] op_sel_hi:[1,0,0]
	v_fma_mix_f32 v46, v233, v83, v46 op_sel:[1,0,0] op_sel_hi:[1,0,0]
	v_fma_mix_f32 v50, v234, v84, v50 op_sel:[0,0,0] op_sel_hi:[1,0,0]
	v_fma_mix_f32 v54, v234, v85, v54 op_sel:[1,0,0] op_sel_hi:[1,0,0]
	v_fma_mix_f32 v58, v235, v86, v58 op_sel:[0,0,0] op_sel_hi:[1,0,0]
	v_fma_mix_f32 v62, v235, v87, v62 op_sel:[1,0,0] op_sel_hi:[1,0,0]
	v_fma_mix_f32 v35, v236, v80, v35 op_sel:[0,0,0] op_sel_hi:[1,0,0]
	v_fma_mix_f32 v39, v236, v81, v39 op_sel:[1,0,0] op_sel_hi:[1,0,0]
	v_fma_mix_f32 v43, v237, v82, v43 op_sel:[0,0,0] op_sel_hi:[1,0,0]
	v_fma_mix_f32 v47, v237, v83, v47 op_sel:[1,0,0] op_sel_hi:[1,0,0]
	v_fma_mix_f32 v51, v238, v84, v51 op_sel:[0,0,0] op_sel_hi:[1,0,0]
	v_fma_mix_f32 v55, v238, v85, v55 op_sel:[1,0,0] op_sel_hi:[1,0,0]
	v_fma_mix_f32 v59, v239, v86, v59 op_sel:[0,0,0] op_sel_hi:[1,0,0]
	v_fma_mix_f32 v63, v239, v87, v63 op_sel:[1,0,0] op_sel_hi:[1,0,0]
	global_store_dwordx4 v154, v[32:35], s[62:63] sc1
	global_store_dwordx4 v154, v[36:39], s[62:63] offset:256 sc1
	global_store_dwordx4 v154, v[40:43], s[62:63] offset:512 sc1
	global_store_dwordx4 v154, v[44:47], s[62:63] offset:768 sc1
	global_store_dwordx4 v154, v[48:51], s[62:63] offset:2048 sc1
	global_store_dwordx4 v154, v[52:55], s[62:63] offset:2304 sc1
	global_store_dwordx4 v154, v[56:59], s[62:63] offset:2560 sc1
	global_store_dwordx4 v154, v[60:63], s[62:63] offset:2816 sc1
	s_waitcnt vmcnt(12)
	v_dot2_f32_f16 v24, v96, v160, 0
	v_dot2_f32_f16 v25, v100, v164, 0
	v_dot2_f32_f16 v26, v104, v168, 0
	v_dot2_f32_f16 v27, v108, v172, 0
	v_dot2_f32_f16 v24, v97, v161, v24
	v_dot2_f32_f16 v25, v101, v165, v25
	v_dot2_f32_f16 v26, v105, v169, v26
	v_dot2_f32_f16 v27, v109, v173, v27
	v_dot2_f32_f16 v24, v98, v162, v24
	v_dot2_f32_f16 v25, v102, v166, v25
	v_dot2_f32_f16 v26, v106, v170, v26
	v_dot2_f32_f16 v27, v110, v174, v27
	v_dot2_f32_f16 v24, v99, v163, v24
	v_dot2_f32_f16 v25, v103, v167, v25
	v_dot2_f32_f16 v26, v107, v171, v26
	v_dot2_f32_f16 v27, v111, v175, v27
	s_waitcnt vmcnt(8)
	v_dot2_f32_f16 v28, v96, v176, 0
	v_dot2_f32_f16 v29, v100, v180, 0
	v_dot2_f32_f16 v30, v104, v184, 0
	v_dot2_f32_f16 v31, v108, v188, 0
	v_dot2_f32_f16 v28, v97, v177, v28
	v_dot2_f32_f16 v29, v101, v181, v29
	v_dot2_f32_f16 v30, v105, v185, v30
	v_dot2_f32_f16 v31, v109, v189, v31
	v_dot2_f32_f16 v28, v98, v178, v28
	v_dot2_f32_f16 v29, v102, v182, v29
	v_dot2_f32_f16 v30, v106, v186, v30
	v_dot2_f32_f16 v31, v110, v190, v31
	v_dot2_f32_f16 v28, v99, v179, v28
	v_dot2_f32_f16 v29, v103, v183, v29
	v_dot2_f32_f16 v30, v107, v187, v30
	v_dot2_f32_f16 v31, v111, v191, v31
	s_nop 2
	v_add_f32_dpp v24, v24, v24 quad_perm:[1,0,3,2] row_mask:0xf bank_mask:0xf
	v_add_f32_dpp v25, v25, v25 quad_perm:[1,0,3,2] row_mask:0xf bank_mask:0xf
	v_add_f32_dpp v26, v26, v26 quad_perm:[1,0,3,2] row_mask:0xf bank_mask:0xf
	v_add_f32_dpp v27, v27, v27 quad_perm:[1,0,3,2] row_mask:0xf bank_mask:0xf
	v_add_f32_dpp v28, v28, v28 quad_perm:[1,0,3,2] row_mask:0xf bank_mask:0xf
	v_add_f32_dpp v29, v29, v29 quad_perm:[1,0,3,2] row_mask:0xf bank_mask:0xf
	v_add_f32_dpp v30, v30, v30 quad_perm:[1,0,3,2] row_mask:0xf bank_mask:0xf
	v_add_f32_dpp v31, v31, v31 quad_perm:[1,0,3,2] row_mask:0xf bank_mask:0xf
	v_add_f32_dpp v24, v24, v24 quad_perm:[2,3,0,1] row_mask:0xf bank_mask:0xf
	v_add_f32_dpp v25, v25, v25 quad_perm:[2,3,0,1] row_mask:0xf bank_mask:0xf
	v_add_f32_dpp v26, v26, v26 quad_perm:[2,3,0,1] row_mask:0xf bank_mask:0xf
	v_add_f32_dpp v27, v27, v27 quad_perm:[2,3,0,1] row_mask:0xf bank_mask:0xf
	v_add_f32_dpp v28, v28, v28 quad_perm:[2,3,0,1] row_mask:0xf bank_mask:0xf
	v_add_f32_dpp v29, v29, v29 quad_perm:[2,3,0,1] row_mask:0xf bank_mask:0xf
	v_add_f32_dpp v30, v30, v30 quad_perm:[2,3,0,1] row_mask:0xf bank_mask:0xf
	v_add_f32_dpp v31, v31, v31 quad_perm:[2,3,0,1] row_mask:0xf bank_mask:0xf
	v_add_f32_dpp v24, v24, v24 row_half_mirror row_mask:0xf bank_mask:0xf
	v_add_f32_dpp v25, v25, v25 row_half_mirror row_mask:0xf bank_mask:0xf
	v_add_f32_dpp v26, v26, v26 row_half_mirror row_mask:0xf bank_mask:0xf
	v_add_f32_dpp v27, v27, v27 row_half_mirror row_mask:0xf bank_mask:0xf
	v_add_f32_dpp v28, v28, v28 row_half_mirror row_mask:0xf bank_mask:0xf
	v_add_f32_dpp v29, v29, v29 row_half_mirror row_mask:0xf bank_mask:0xf
	v_add_f32_dpp v30, v30, v30 row_half_mirror row_mask:0xf bank_mask:0xf
	v_add_f32_dpp v31, v31, v31 row_half_mirror row_mask:0xf bank_mask:0xf
	v_cndmask_b32_e64 v115, v24, v25, s[70:71]
	v_cndmask_b32_e64 v116, v28, v29, s[70:71]
	v_cndmask_b32_e64 v115, v115, v26, s[72:73]
	v_cndmask_b32_e64 v116, v116, v30, s[72:73]
	v_cndmask_b32_e64 v115, v115, v27, s[74:75]
	v_cndmask_b32_e64 v116, v116, v31, s[74:75]
	v_add_f32_e32 v115, 0x42659caf, v115
	v_add_f32_e32 v116, 0x42659caf, v116
	v_add_f32_e32 v115, s42, v115
	v_add_f32_e32 v116, s43, v116
	v_max_f32_e32 v118, v115, v116
	v_sub_f32_e32 v118, v118, v117
	v_cmp_ngt_f32_e32 vcc, s30, v118
	s_cmp_lg_u64 vcc, 0
	s_cselect_b32 s26, 1, 0
	s_or_b32 s31, s31, s26
	s_lshl_b32 s26, s19, 2
	s_add_i32 s26, s26, 0x20700
	v_mov_b32_e32 v139, s26
	v_mov_b32_e32 v140, s31
	ds_write_b32 v139, v140
	s_waitcnt lgkmcnt(0)
	s_barrier
	v_mov_b32_e32 v139, 0x20700
	ds_read_b128 v[144:147], v139
	ds_read_b128 v[148:151], v139 offset:16
	s_waitcnt lgkmcnt(0)
	v_or3_b32 v144, v144, v145, v146
	v_or3_b32 v148, v148, v149, v150
	v_or3_b32 v144, v144, v147, v148
	v_or_b32_e32 v144, v144, v151
	s_nop 0
	v_readfirstlane_b32 s27, v144
	s_nop 3
	s_cmp_lg_u32 s27, 0
	s_cbranch_scc1 .Lattn_fallback
	s_endpgm
